# speedup vs baseline: 1.0030x; 1.0030x over previous
.LBB7_27:
	ds_read_b128 v[128:131], v170
	ds_read_b128 v[132:135], v170 offset:1024
	ds_read_b128 v[136:139], v170 offset:2048
	ds_read_b128 v[140:143], v170 offset:3072
	s_add_u32 s30, s28, 0xfffd0080
	s_addc_u32 s31, s29, -1
	s_cmp_eq_u32 s73, 8
	s_cselect_b32 s35, s9, s31
	s_cselect_b32 s34, s8, s30
	s_cselect_b32 s31, s1, s72
	s_cselect_b32 s30, s0, s71
	v_lshl_add_u64 v[162:163], s[28:29], 0, v[152:153]
	s_add_i32 m0, s43, 0xc000
	ds_read_b128 v[158:161], v171
	ds_read_b128 v[176:179], v171 offset:1024
	ds_read_b128 v[180:183], v171 offset:2048
	ds_read_b128 v[184:187], v171 offset:3072
	ds_read_b128 v[188:191], v171 offset:4096
	ds_read_b128 v[192:195], v171 offset:5120
	ds_read_b128 v[196:199], v171 offset:6144
	ds_read_b128 v[200:203], v171 offset:7168
	global_load_lds_dwordx4 v[162:163], off
	v_lshl_add_u64 v[162:163], s[28:29], 0, v[154:155]
	s_add_i32 m0, s43, 0xe000
	s_nop 0
	global_load_lds_dwordx4 v[162:163], off
	s_waitcnt lgkmcnt(8)
	s_barrier
	s_waitcnt lgkmcnt(0)
	s_setprio 1
	s_waitcnt lgkmcnt(0)
	v_mfma_f32_16x16x32_f16 v[124:127], v[128:131], v[158:161], v[124:127]
	v_mfma_f32_16x16x32_f16 v[120:123], v[136:139], v[158:161], v[120:123]
	v_mfma_f32_16x16x32_f16 v[108:111], v[128:131], v[180:183], v[108:111]
	v_mfma_f32_16x16x32_f16 v[104:107], v[136:139], v[180:183], v[104:107]
	v_mfma_f32_16x16x32_f16 v[96:99], v[128:131], v[188:191], v[96:99]
	v_mfma_f32_16x16x32_f16 v[88:91], v[136:139], v[188:191], v[88:91]
	v_mfma_f32_16x16x32_f16 v[80:83], v[128:131], v[196:199], v[80:83]
	v_mfma_f32_16x16x32_f16 v[72:75], v[136:139], v[196:199], v[72:75]
	v_mfma_f32_16x16x32_f16 v[124:127], v[132:135], v[176:179], v[124:127]
	v_mfma_f32_16x16x32_f16 v[120:123], v[140:143], v[176:179], v[120:123]
	v_mfma_f32_16x16x32_f16 v[108:111], v[132:135], v[184:187], v[108:111]
	v_mfma_f32_16x16x32_f16 v[104:107], v[140:143], v[184:187], v[104:107]
	v_mfma_f32_16x16x32_f16 v[96:99], v[132:135], v[192:195], v[96:99]
	v_mfma_f32_16x16x32_f16 v[88:91], v[140:143], v[192:195], v[88:91]
	v_mfma_f32_16x16x32_f16 v[80:83], v[132:135], v[200:203], v[80:83]
	v_mfma_f32_16x16x32_f16 v[72:75], v[140:143], v[200:203], v[72:75]
	s_setprio 0
	s_barrier
	s_add_i32 s74, s65, s42
	v_lshl_add_u64 v[162:163], s[30:31], 0, v[146:147]
	s_mov_b32 m0, s74
	ds_read_b128 v[204:207], v172
	ds_read_b128 v[208:211], v172 offset:1024
	ds_read_b128 v[212:215], v172 offset:2048
	ds_read_b128 v[216:219], v172 offset:3072
	global_load_lds_dwordx4 v[162:163], off
	v_lshl_add_u64 v[220:221], s[30:31], 0, v[150:151]
	s_add_i32 m0, s74, 0x2000
	s_nop 0
	global_load_lds_dwordx4 v[220:221], off
	s_barrier
	s_waitcnt lgkmcnt(0)
	s_setprio 1
	s_waitcnt lgkmcnt(0)
	v_mfma_f32_16x16x32_f16 v[116:119], v[204:207], v[158:161], v[116:119]
	v_mfma_f32_16x16x32_f16 v[112:115], v[212:215], v[158:161], v[112:115]
	v_mfma_f32_16x16x32_f16 v[100:103], v[204:207], v[180:183], v[100:103]
	v_mfma_f32_16x16x32_f16 v[92:95], v[212:215], v[180:183], v[92:95]
	v_mfma_f32_16x16x32_f16 v[84:87], v[204:207], v[188:191], v[84:87]
	v_mfma_f32_16x16x32_f16 v[76:79], v[212:215], v[188:191], v[76:79]
	v_mfma_f32_16x16x32_f16 v[68:71], v[204:207], v[196:199], v[68:71]
	v_mfma_f32_16x16x32_f16 v[64:67], v[212:215], v[196:199], v[64:67]
	v_mfma_f32_16x16x32_f16 v[116:119], v[208:211], v[176:179], v[116:119]
	v_mfma_f32_16x16x32_f16 v[112:115], v[216:219], v[176:179], v[112:115]
	v_mfma_f32_16x16x32_f16 v[100:103], v[208:211], v[184:187], v[100:103]
	v_mfma_f32_16x16x32_f16 v[92:95], v[216:219], v[184:187], v[92:95]
	v_mfma_f32_16x16x32_f16 v[84:87], v[208:211], v[192:195], v[84:87]
	v_mfma_f32_16x16x32_f16 v[76:79], v[216:219], v[192:195], v[76:79]
	v_mfma_f32_16x16x32_f16 v[68:71], v[208:211], v[200:203], v[68:71]
	v_mfma_f32_16x16x32_f16 v[64:67], v[216:219], v[200:203], v[64:67]
	s_setprio 0
	s_mov_b32 m0, s43
	v_lshl_add_u64 v[222:223], s[34:35], 0, v[144:145]
	s_barrier
	ds_read_b128 v[158:161], v171 offset:16384
	ds_read_b128 v[176:179], v171 offset:17408
	ds_read_b128 v[180:183], v171 offset:18432
	ds_read_b128 v[184:187], v171 offset:19456
	ds_read_b128 v[188:191], v171 offset:20480
	ds_read_b128 v[192:195], v171 offset:21504
	ds_read_b128 v[196:199], v171 offset:22528
	ds_read_b128 v[200:203], v171 offset:23552
	global_load_lds_dwordx4 v[222:223], off
	v_lshl_add_u64 v[224:225], s[34:35], 0, v[148:149]
	s_mov_b32 m0, s44
	s_nop 0
	global_load_lds_dwordx4 v[224:225], off
	s_barrier
	s_waitcnt lgkmcnt(0)
	s_setprio 1
	s_waitcnt lgkmcnt(0)
	v_mfma_f32_16x16x32_f16 v[60:63], v[128:131], v[158:161], v[60:63]
	v_mfma_f32_16x16x32_f16 v[56:59], v[136:139], v[158:161], v[56:59]
	v_mfma_f32_16x16x32_f16 v[48:51], v[128:131], v[180:183], v[48:51]
	v_mfma_f32_16x16x32_f16 v[40:43], v[136:139], v[180:183], v[40:43]
	v_mfma_f32_16x16x32_f16 v[32:35], v[128:131], v[188:191], v[32:35]
	v_mfma_f32_16x16x32_f16 v[24:27], v[136:139], v[188:191], v[24:27]
	v_mfma_f32_16x16x32_f16 v[16:19], v[128:131], v[196:199], v[16:19]
	v_mfma_f32_16x16x32_f16 v[8:11], v[136:139], v[196:199], v[8:11]
	v_mfma_f32_16x16x32_f16 v[60:63], v[132:135], v[176:179], v[60:63]
	v_mfma_f32_16x16x32_f16 v[56:59], v[140:143], v[176:179], v[56:59]
	v_mfma_f32_16x16x32_f16 v[48:51], v[132:135], v[184:187], v[48:51]
	v_mfma_f32_16x16x32_f16 v[40:43], v[140:143], v[184:187], v[40:43]
	v_mfma_f32_16x16x32_f16 v[32:35], v[132:135], v[192:195], v[32:35]
	v_mfma_f32_16x16x32_f16 v[24:27], v[140:143], v[192:195], v[24:27]
	v_mfma_f32_16x16x32_f16 v[16:19], v[132:135], v[200:203], v[16:19]
	v_mfma_f32_16x16x32_f16 v[8:11], v[140:143], v[200:203], v[8:11]
	s_setprio 0
	s_barrier
	s_add_u32 s74, s30, 0xc000
	s_addc_u32 s75, s31, 0
	s_add_i32 s76, s66, s42
	v_lshl_add_u64 v[128:129], s[74:75], 0, v[146:147]
	s_mov_b32 m0, s76
	s_nop 0
	global_load_lds_dwordx4 v[128:129], off
	v_lshl_add_u64 v[128:129], s[74:75], 0, v[150:151]
	s_add_i32 m0, s76, 0x2000
	s_nop 0
	global_load_lds_dwordx4 v[128:129], off
	s_waitcnt vmcnt(6)
	s_barrier
	s_setprio 1
	v_mfma_f32_16x16x32_f16 v[52:55], v[204:207], v[158:161], v[52:55]
	v_mfma_f32_16x16x32_f16 v[44:47], v[212:215], v[158:161], v[44:47]
	v_mfma_f32_16x16x32_f16 v[36:39], v[204:207], v[180:183], v[36:39]
	v_mfma_f32_16x16x32_f16 v[28:31], v[212:215], v[180:183], v[28:31]
	v_mfma_f32_16x16x32_f16 v[20:23], v[204:207], v[188:191], v[20:23]
	v_mfma_f32_16x16x32_f16 v[12:15], v[212:215], v[188:191], v[12:15]
	v_mfma_f32_16x16x32_f16 v[4:7], v[204:207], v[196:199], v[4:7]
	v_mfma_f32_16x16x32_f16 v[0:3], v[212:215], v[196:199], v[0:3]
	v_mfma_f32_16x16x32_f16 v[52:55], v[208:211], v[176:179], v[52:55]
	v_mfma_f32_16x16x32_f16 v[44:47], v[216:219], v[176:179], v[44:47]
	v_mfma_f32_16x16x32_f16 v[36:39], v[208:211], v[184:187], v[36:39]
	v_mfma_f32_16x16x32_f16 v[28:31], v[216:219], v[184:187], v[28:31]
	v_mfma_f32_16x16x32_f16 v[20:23], v[208:211], v[192:195], v[20:23]
	v_mfma_f32_16x16x32_f16 v[12:15], v[216:219], v[192:195], v[12:15]
	v_mfma_f32_16x16x32_f16 v[4:7], v[208:211], v[200:203], v[4:7]
	v_mfma_f32_16x16x32_f16 v[0:3], v[216:219], v[200:203], v[0:3]
	s_setprio 0
	s_add_i32 s74, 0, 0x18000
	v_add_u32_e32 v140, s74, v166
	s_barrier
	ds_read_b128 v[128:131], v140
	ds_read_b128 v[132:135], v140 offset:1024
	ds_read_b128 v[136:139], v140 offset:2048
	ds_read_b128 v[140:143], v140 offset:3072
	s_add_u32 s34, s34, 0x30000
	s_addc_u32 s35, s35, 0
	s_mov_b32 m0, s45
	v_lshl_add_u64 v[204:205], s[34:35], 0, v[144:145]
	ds_read_b128 v[158:161], v171 offset:32768
	ds_read_b128 v[176:179], v171 offset:33792
	ds_read_b128 v[180:183], v171 offset:34816
	ds_read_b128 v[184:187], v171 offset:35840
	ds_read_b128 v[188:191], v171 offset:36864
	ds_read_b128 v[192:195], v171 offset:37888
	ds_read_b128 v[196:199], v171 offset:38912
	ds_read_b128 v[200:203], v171 offset:39936
	global_load_lds_dwordx4 v[204:205], off
	v_lshl_add_u64 v[204:205], s[34:35], 0, v[148:149]
	s_mov_b32 m0, s46
	s_nop 0
	global_load_lds_dwordx4 v[204:205], off
	s_waitcnt lgkmcnt(8)
	s_barrier
	s_waitcnt lgkmcnt(0)
	s_setprio 1
	s_waitcnt lgkmcnt(0)
	v_mfma_f32_16x16x32_f16 v[124:127], v[128:131], v[158:161], v[124:127]
	v_mfma_f32_16x16x32_f16 v[120:123], v[136:139], v[158:161], v[120:123]
	v_mfma_f32_16x16x32_f16 v[108:111], v[128:131], v[180:183], v[108:111]
	v_mfma_f32_16x16x32_f16 v[104:107], v[136:139], v[180:183], v[104:107]
	v_mfma_f32_16x16x32_f16 v[96:99], v[128:131], v[188:191], v[96:99]
	v_mfma_f32_16x16x32_f16 v[88:91], v[136:139], v[188:191], v[88:91]
	v_mfma_f32_16x16x32_f16 v[80:83], v[128:131], v[196:199], v[80:83]
	v_mfma_f32_16x16x32_f16 v[72:75], v[136:139], v[196:199], v[72:75]
	v_mfma_f32_16x16x32_f16 v[124:127], v[132:135], v[176:179], v[124:127]
	v_mfma_f32_16x16x32_f16 v[120:123], v[140:143], v[176:179], v[120:123]
	v_mfma_f32_16x16x32_f16 v[108:111], v[132:135], v[184:187], v[108:111]
	v_mfma_f32_16x16x32_f16 v[104:107], v[140:143], v[184:187], v[104:107]
	v_mfma_f32_16x16x32_f16 v[96:99], v[132:135], v[192:195], v[96:99]
	v_mfma_f32_16x16x32_f16 v[88:91], v[140:143], v[192:195], v[88:91]
	v_mfma_f32_16x16x32_f16 v[80:83], v[132:135], v[200:203], v[80:83]
	v_mfma_f32_16x16x32_f16 v[72:75], v[140:143], v[200:203], v[72:75]
	s_setprio 0
	s_barrier
	s_add_i32 s34, 0, 0x1c000
	s_add_i32 s35, s74, s42
	v_add_u32_e32 v175, s34, v166
	v_lshl_add_u64 v[162:163], v[162:163], 0, s[26:27]
	s_mov_b32 m0, s35
	ds_read_b128 v[204:207], v175
	ds_read_b128 v[208:211], v175 offset:1024
	ds_read_b128 v[212:215], v175 offset:2048
	ds_read_b128 v[216:219], v175 offset:3072
	global_load_lds_dwordx4 v[162:163], off
	v_lshl_add_u64 v[162:163], v[220:221], 0, s[26:27]
	s_add_i32 m0, s35, 0x2000
	s_nop 0
	global_load_lds_dwordx4 v[162:163], off
	s_barrier
	s_waitcnt lgkmcnt(0)
	s_setprio 1
	s_waitcnt lgkmcnt(0)
	v_mfma_f32_16x16x32_f16 v[116:119], v[204:207], v[158:161], v[116:119]
	v_mfma_f32_16x16x32_f16 v[112:115], v[212:215], v[158:161], v[112:115]
	v_mfma_f32_16x16x32_f16 v[100:103], v[204:207], v[180:183], v[100:103]
	v_mfma_f32_16x16x32_f16 v[92:95], v[212:215], v[180:183], v[92:95]
	v_mfma_f32_16x16x32_f16 v[84:87], v[204:207], v[188:191], v[84:87]
	v_mfma_f32_16x16x32_f16 v[76:79], v[212:215], v[188:191], v[76:79]
	v_mfma_f32_16x16x32_f16 v[68:71], v[204:207], v[196:199], v[68:71]
	v_mfma_f32_16x16x32_f16 v[64:67], v[212:215], v[196:199], v[64:67]
	v_mfma_f32_16x16x32_f16 v[116:119], v[208:211], v[176:179], v[116:119]
	v_mfma_f32_16x16x32_f16 v[112:115], v[216:219], v[176:179], v[112:115]
	v_mfma_f32_16x16x32_f16 v[100:103], v[208:211], v[184:187], v[100:103]
	v_mfma_f32_16x16x32_f16 v[92:95], v[216:219], v[184:187], v[92:95]
	v_mfma_f32_16x16x32_f16 v[84:87], v[208:211], v[192:195], v[84:87]
	v_mfma_f32_16x16x32_f16 v[76:79], v[216:219], v[192:195], v[76:79]
	v_mfma_f32_16x16x32_f16 v[68:71], v[208:211], v[200:203], v[68:71]
	v_mfma_f32_16x16x32_f16 v[64:67], v[216:219], v[200:203], v[64:67]
	s_setprio 0
	s_mov_b32 m0, s49
	v_lshl_add_u64 v[162:163], v[222:223], 0, s[26:27]
	s_barrier
	ds_read_b128 v[158:161], v171 offset:49152
	ds_read_b128 v[176:179], v171 offset:50176
	ds_read_b128 v[180:183], v171 offset:51200
	ds_read_b128 v[184:187], v171 offset:52224
	ds_read_b128 v[188:191], v171 offset:53248
	ds_read_b128 v[192:195], v171 offset:54272
	ds_read_b128 v[196:199], v171 offset:55296
	ds_read_b128 v[200:203], v171 offset:56320
	global_load_lds_dwordx4 v[162:163], off
	v_lshl_add_u64 v[162:163], v[224:225], 0, s[26:27]
	s_mov_b32 m0, s50
	s_nop 0
	global_load_lds_dwordx4 v[162:163], off
	s_barrier
	s_waitcnt lgkmcnt(0)
	s_setprio 1
	s_waitcnt lgkmcnt(0)
	v_mfma_f32_16x16x32_f16 v[60:63], v[128:131], v[158:161], v[60:63]
	v_mfma_f32_16x16x32_f16 v[56:59], v[136:139], v[158:161], v[56:59]
	v_mfma_f32_16x16x32_f16 v[48:51], v[128:131], v[180:183], v[48:51]
	v_mfma_f32_16x16x32_f16 v[40:43], v[136:139], v[180:183], v[40:43]
	v_mfma_f32_16x16x32_f16 v[32:35], v[128:131], v[188:191], v[32:35]
	v_mfma_f32_16x16x32_f16 v[24:27], v[136:139], v[188:191], v[24:27]
	v_mfma_f32_16x16x32_f16 v[16:19], v[128:131], v[196:199], v[16:19]
	v_mfma_f32_16x16x32_f16 v[8:11], v[136:139], v[196:199], v[8:11]
	v_mfma_f32_16x16x32_f16 v[60:63], v[132:135], v[176:179], v[60:63]
	v_mfma_f32_16x16x32_f16 v[56:59], v[140:143], v[176:179], v[56:59]
	v_mfma_f32_16x16x32_f16 v[48:51], v[132:135], v[184:187], v[48:51]
	v_mfma_f32_16x16x32_f16 v[40:43], v[140:143], v[184:187], v[40:43]
	v_mfma_f32_16x16x32_f16 v[32:35], v[132:135], v[192:195], v[32:35]
	v_mfma_f32_16x16x32_f16 v[24:27], v[140:143], v[192:195], v[24:27]
	v_mfma_f32_16x16x32_f16 v[16:19], v[132:135], v[200:203], v[16:19]
	v_mfma_f32_16x16x32_f16 v[8:11], v[140:143], v[200:203], v[8:11]
	s_setprio 0
	s_barrier
	s_add_u32 s30, s30, 0xc080
	s_addc_u32 s31, s31, 0
	s_add_i32 s34, s34, s42
	v_lshl_add_u64 v[128:129], s[30:31], 0, v[146:147]
	s_mov_b32 m0, s34
	s_nop 0
	global_load_lds_dwordx4 v[128:129], off
	v_lshl_add_u64 v[128:129], s[30:31], 0, v[150:151]
	s_add_i32 m0, s34, 0x2000
	s_nop 0
	global_load_lds_dwordx4 v[128:129], off
	s_waitcnt vmcnt(6)
	s_barrier
	s_setprio 1
	v_mfma_f32_16x16x32_f16 v[52:55], v[204:207], v[158:161], v[52:55]
	v_mfma_f32_16x16x32_f16 v[44:47], v[212:215], v[158:161], v[44:47]
	v_mfma_f32_16x16x32_f16 v[36:39], v[204:207], v[180:183], v[36:39]
	v_mfma_f32_16x16x32_f16 v[28:31], v[212:215], v[180:183], v[28:31]
	v_mfma_f32_16x16x32_f16 v[20:23], v[204:207], v[188:191], v[20:23]
	v_mfma_f32_16x16x32_f16 v[12:15], v[212:215], v[188:191], v[12:15]
	v_mfma_f32_16x16x32_f16 v[4:7], v[204:207], v[196:199], v[4:7]
	v_mfma_f32_16x16x32_f16 v[0:3], v[212:215], v[196:199], v[0:3]
	v_mfma_f32_16x16x32_f16 v[52:55], v[208:211], v[176:179], v[52:55]
	v_mfma_f32_16x16x32_f16 v[44:47], v[216:219], v[176:179], v[44:47]
	v_mfma_f32_16x16x32_f16 v[36:39], v[208:211], v[184:187], v[36:39]
	v_mfma_f32_16x16x32_f16 v[28:31], v[216:219], v[184:187], v[28:31]
	v_mfma_f32_16x16x32_f16 v[20:23], v[208:211], v[192:195], v[20:23]
	v_mfma_f32_16x16x32_f16 v[12:15], v[216:219], v[192:195], v[12:15]
	v_mfma_f32_16x16x32_f16 v[4:7], v[208:211], v[200:203], v[4:7]
	v_mfma_f32_16x16x32_f16 v[0:3], v[216:219], v[200:203], v[0:3]
	s_setprio 0
	s_add_i32 s73, s73, 2
	s_add_u32 s28, s28, 0x100
	s_addc_u32 s29, s29, 0
	s_add_u32 s71, s71, 0x100
	s_addc_u32 s72, s72, 0
	s_cmp_gt_u32 s73, 9
	s_barrier
	s_cbranch_scc0 .LBB7_27
	s_lshl_b32 s28, s70, 8
	s_add_i32 s28, s28, s48
	s_lshl_b32 s29, s67, 8
	s_or_b32 s29, s29, s51
	s_waitcnt vmcnt(6)
	v_pk_fma_f32 v[126:127], v[126:127], v[226:227], v[236:237] op_sel_hi:[1,0,1]
	v_pk_fma_f32 v[124:125], v[124:125], v[226:227], v[234:235] op_sel_hi:[1,0,1]
	v_pk_fma_f32 v[186:187], v[122:123], v[226:227], v[240:241] op_sel_hi:[1,0,1]
	v_pk_fma_f32 v[122:123], v[120:121], v[226:227], v[238:239] op_sel_hi:[1,0,1]
	v_cvt_pk_f16_f32 v120, v124, v125
	v_cvt_pk_f16_f32 v121, v126, v127
	v_cvt_pk_f16_f32 v122, v122, v123
	v_cvt_pk_f16_f32 v123, v186, v187
	ds_write_b128 v173, v[120:123]
	v_pk_fma_f32 v[118:119], v[118:119], v[226:227], v[244:245] op_sel_hi:[1,0,1]
	v_pk_fma_f32 v[116:117], v[116:117], v[226:227], v[242:243] op_sel_hi:[1,0,1]
	v_pk_fma_f32 v[120:121], v[114:115], v[226:227], v[248:249] op_sel_hi:[1,0,1]
	v_pk_fma_f32 v[114:115], v[112:113], v[226:227], v[246:247] op_sel_hi:[1,0,1]
	v_cvt_pk_f16_f32 v112, v116, v117
	v_cvt_pk_f16_f32 v113, v118, v119
	v_cvt_pk_f16_f32 v114, v114, v115
	v_cvt_pk_f16_f32 v115, v120, v121
	ds_write_b128 v173, v[112:115] offset:64
	v_or_b32_e32 v116, s28, v167
	ds_read_b128 v[112:115], v174
	v_mul_lo_u32 v116, v116, s10
	v_add_u32_e32 v120, s29, v116
	v_lshlrev_b32_e32 v121, 1, v120
	v_add_u32_e32 v122, v121, v168
	ds_read_b128 v[116:119], v174 offset:1152
	s_waitcnt lgkmcnt(0)
	buffer_store_dwordx4 v[112:115], v122, s[20:23], 0 offen
	v_pk_fma_f32 v[110:111], v[110:111], v[226:227], v[236:237] op_sel:[0,1,0]
	v_pk_fma_f32 v[108:109], v[108:109], v[226:227], v[234:235] op_sel:[0,1,0]
	v_pk_fma_f32 v[112:113], v[106:107], v[226:227], v[240:241] op_sel:[0,1,0]
	v_pk_fma_f32 v[106:107], v[104:105], v[226:227], v[238:239] op_sel:[0,1,0]
	v_cvt_pk_f16_f32 v104, v108, v109
	v_cvt_pk_f16_f32 v105, v110, v111
	v_cvt_pk_f16_f32 v106, v106, v107
	v_cvt_pk_f16_f32 v107, v112, v113
	ds_write_b128 v173, v[104:107]
	v_pk_fma_f32 v[102:103], v[102:103], v[226:227], v[244:245] op_sel:[0,1,0]
	v_pk_fma_f32 v[100:101], v[100:101], v[226:227], v[242:243] op_sel:[0,1,0]
	v_pk_fma_f32 v[104:105], v[94:95], v[226:227], v[248:249] op_sel:[0,1,0]
	v_pk_fma_f32 v[94:95], v[92:93], v[226:227], v[246:247] op_sel:[0,1,0]
	v_cvt_pk_f16_f32 v92, v100, v101
	v_cvt_pk_f16_f32 v93, v102, v103
	v_cvt_pk_f16_f32 v94, v94, v95
	v_cvt_pk_f16_f32 v95, v104, v105
	ds_write_b128 v173, v[92:95] offset:64
	ds_read_b128 v[92:95], v174
	ds_read_b128 v[100:103], v174 offset:1152
	v_add_u32_e32 v104, s55, v121
	v_add_u32_e32 v114, v121, v169
	v_add_u32_e32 v105, v104, v168
	buffer_store_dwordx4 v[116:119], v114, s[20:23], 0 offen
	s_waitcnt lgkmcnt(1)
	buffer_store_dwordx4 v[92:95], v105, s[20:23], 0 offen
	v_pk_fma_f32 v[86:87], v[86:87], v[228:229], v[244:245] op_sel_hi:[1,0,1]
	v_pk_fma_f32 v[84:85], v[84:85], v[228:229], v[242:243] op_sel_hi:[1,0,1]
	v_pk_fma_f32 v[92:93], v[98:99], v[228:229], v[236:237] op_sel_hi:[1,0,1]
	v_pk_fma_f32 v[94:95], v[96:97], v[228:229], v[234:235] op_sel_hi:[1,0,1]
	v_pk_fma_f32 v[96:97], v[90:91], v[228:229], v[240:241] op_sel_hi:[1,0,1]
	v_pk_fma_f32 v[90:91], v[88:89], v[228:229], v[238:239] op_sel_hi:[1,0,1]
	v_cvt_pk_f16_f32 v88, v94, v95
	v_cvt_pk_f16_f32 v89, v92, v93
	v_cvt_pk_f16_f32 v90, v90, v91
	v_cvt_pk_f16_f32 v91, v96, v97
	ds_write_b128 v173, v[88:91]
	v_pk_fma_f32 v[88:89], v[78:79], v[228:229], v[248:249] op_sel_hi:[1,0,1]
	v_pk_fma_f32 v[78:79], v[76:77], v[228:229], v[246:247] op_sel_hi:[1,0,1]
	v_cvt_pk_f16_f32 v76, v84, v85
	v_cvt_pk_f16_f32 v77, v86, v87
	v_cvt_pk_f16_f32 v78, v78, v79
	v_cvt_pk_f16_f32 v79, v88, v89
	ds_write_b128 v173, v[76:79] offset:64
	ds_read_b128 v[76:79], v174
	ds_read_b128 v[84:87], v174 offset:1152
	v_add_u32_e32 v88, s55, v104
	v_add_u32_e32 v105, v104, v169
	v_add_u32_e32 v89, v88, v168
	s_waitcnt lgkmcnt(4)
	buffer_store_dwordx4 v[100:103], v105, s[20:23], 0 offen
	s_waitcnt lgkmcnt(1)
	buffer_store_dwordx4 v[76:79], v89, s[20:23], 0 offen
	v_pk_fma_f32 v[70:71], v[70:71], v[228:229], v[244:245] op_sel:[0,1,0]
	v_pk_fma_f32 v[68:69], v[68:69], v[228:229], v[242:243] op_sel:[0,1,0]
	v_add_u32_e32 v76, v88, v169
	s_waitcnt lgkmcnt(0)
	buffer_store_dwordx4 v[84:87], v76, s[20:23], 0 offen
	v_pk_fma_f32 v[76:77], v[82:83], v[228:229], v[236:237] op_sel:[0,1,0]
	v_pk_fma_f32 v[78:79], v[80:81], v[228:229], v[234:235] op_sel:[0,1,0]
	v_pk_fma_f32 v[80:81], v[74:75], v[228:229], v[240:241] op_sel:[0,1,0]
	v_pk_fma_f32 v[74:75], v[72:73], v[228:229], v[238:239] op_sel:[0,1,0]
	v_cvt_pk_f16_f32 v72, v78, v79
	v_cvt_pk_f16_f32 v73, v76, v77
	v_cvt_pk_f16_f32 v74, v74, v75
	v_cvt_pk_f16_f32 v75, v80, v81
	ds_write_b128 v173, v[72:75]
	v_pk_fma_f32 v[72:73], v[66:67], v[228:229], v[248:249] op_sel:[0,1,0]
	v_pk_fma_f32 v[66:67], v[64:65], v[228:229], v[246:247] op_sel:[0,1,0]
	v_cvt_pk_f16_f32 v64, v68, v69
	v_cvt_pk_f16_f32 v65, v70, v71
	v_cvt_pk_f16_f32 v66, v66, v67
	v_cvt_pk_f16_f32 v67, v72, v73
	ds_write_b128 v173, v[64:67] offset:64
	ds_read_b128 v[64:67], v174
	ds_read_b128 v[68:71], v174 offset:1152
	v_add_u32_e32 v72, s56, v120
	v_lshlrev_b32_e32 v73, 1, v72
	v_add_u32_e32 v74, v73, v168
	s_waitcnt lgkmcnt(1)
	buffer_store_dwordx4 v[64:67], v74, s[20:23], 0 offen
	v_pk_fma_f32 v[62:63], v[62:63], v[230:231], v[236:237] op_sel_hi:[1,0,1]
	v_pk_fma_f32 v[60:61], v[60:61], v[230:231], v[234:235] op_sel_hi:[1,0,1]
	v_pk_fma_f32 v[64:65], v[58:59], v[230:231], v[240:241] op_sel_hi:[1,0,1]
	v_pk_fma_f32 v[58:59], v[56:57], v[230:231], v[238:239] op_sel_hi:[1,0,1]
	v_cvt_pk_f16_f32 v56, v60, v61
	v_cvt_pk_f16_f32 v57, v62, v63
	v_cvt_pk_f16_f32 v58, v58, v59
	v_cvt_pk_f16_f32 v59, v64, v65
	ds_write_b128 v173, v[56:59]
	v_pk_fma_f32 v[54:55], v[54:55], v[230:231], v[244:245] op_sel_hi:[1,0,1]
	v_pk_fma_f32 v[52:53], v[52:53], v[230:231], v[242:243] op_sel_hi:[1,0,1]
	v_pk_fma_f32 v[56:57], v[46:47], v[230:231], v[248:249] op_sel_hi:[1,0,1]
	v_pk_fma_f32 v[46:47], v[44:45], v[230:231], v[246:247] op_sel_hi:[1,0,1]
	v_cvt_pk_f16_f32 v44, v52, v53
	v_cvt_pk_f16_f32 v45, v54, v55
	v_cvt_pk_f16_f32 v46, v46, v47
	v_cvt_pk_f16_f32 v47, v56, v57
	ds_write_b128 v173, v[44:47] offset:64
	ds_read_b128 v[44:47], v174
	ds_read_b128 v[52:55], v174 offset:1152
	v_add_u32_e32 v56, s62, v88
	v_add_u32_e32 v66, v73, v169
	v_add_u32_e32 v57, v56, v168
	s_waitcnt lgkmcnt(4)
	buffer_store_dwordx4 v[68:71], v66, s[20:23], 0 offen
	s_waitcnt lgkmcnt(1)
	buffer_store_dwordx4 v[44:47], v57, s[20:23], 0 offen
	v_pk_fma_f32 v[38:39], v[38:39], v[230:231], v[244:245] op_sel:[0,1,0]
	v_pk_fma_f32 v[36:37], v[36:37], v[230:231], v[242:243] op_sel:[0,1,0]
	v_add_u32_e32 v44, v56, v169
	s_waitcnt lgkmcnt(0)
	buffer_store_dwordx4 v[52:55], v44, s[20:23], 0 offen
	v_pk_fma_f32 v[44:45], v[50:51], v[230:231], v[236:237] op_sel:[0,1,0]
	v_pk_fma_f32 v[46:47], v[48:49], v[230:231], v[234:235] op_sel:[0,1,0]
	v_pk_fma_f32 v[48:49], v[42:43], v[230:231], v[240:241] op_sel:[0,1,0]
	v_pk_fma_f32 v[42:43], v[40:41], v[230:231], v[238:239] op_sel:[0,1,0]
	v_cvt_pk_f16_f32 v40, v46, v47
	v_cvt_pk_f16_f32 v41, v44, v45
	v_cvt_pk_f16_f32 v42, v42, v43
	v_cvt_pk_f16_f32 v43, v48, v49
	ds_write_b128 v173, v[40:43]
	v_pk_fma_f32 v[40:41], v[30:31], v[230:231], v[248:249] op_sel:[0,1,0]
	v_pk_fma_f32 v[30:31], v[28:29], v[230:231], v[246:247] op_sel:[0,1,0]
	v_cvt_pk_f16_f32 v28, v36, v37
	v_cvt_pk_f16_f32 v29, v38, v39
	v_cvt_pk_f16_f32 v30, v30, v31
	v_cvt_pk_f16_f32 v31, v40, v41
	ds_write_b128 v173, v[28:31] offset:64
	ds_read_b128 v[28:31], v174
	ds_read_b128 v[36:39], v174 offset:1152
	v_add_u32_e32 v40, s63, v72
	v_lshlrev_b32_e32 v41, 1, v40
	v_add_u32_e32 v42, v41, v168
	s_waitcnt lgkmcnt(1)
	buffer_store_dwordx4 v[28:31], v42, s[20:23], 0 offen
	v_pk_fma_f32 v[22:23], v[22:23], v[232:233], v[244:245] op_sel_hi:[1,0,1]
	v_pk_fma_f32 v[20:21], v[20:21], v[232:233], v[242:243] op_sel_hi:[1,0,1]
	v_add_u32_e32 v28, v41, v169
	s_waitcnt lgkmcnt(0)
	buffer_store_dwordx4 v[36:39], v28, s[20:23], 0 offen
	v_pk_fma_f32 v[28:29], v[34:35], v[232:233], v[236:237] op_sel_hi:[1,0,1]
	v_pk_fma_f32 v[30:31], v[32:33], v[232:233], v[234:235] op_sel_hi:[1,0,1]
	v_pk_fma_f32 v[32:33], v[26:27], v[232:233], v[240:241] op_sel_hi:[1,0,1]
	v_pk_fma_f32 v[26:27], v[24:25], v[232:233], v[238:239] op_sel_hi:[1,0,1]
	v_cvt_pk_f16_f32 v24, v30, v31
	v_cvt_pk_f16_f32 v25, v28, v29
	v_cvt_pk_f16_f32 v26, v26, v27
	v_cvt_pk_f16_f32 v27, v32, v33
	ds_write_b128 v173, v[24:27]
	v_pk_fma_f32 v[24:25], v[14:15], v[232:233], v[248:249] op_sel_hi:[1,0,1]
	v_pk_fma_f32 v[14:15], v[12:13], v[232:233], v[246:247] op_sel_hi:[1,0,1]
	v_cvt_pk_f16_f32 v12, v20, v21
	v_cvt_pk_f16_f32 v13, v22, v23
	v_cvt_pk_f16_f32 v14, v14, v15
	v_cvt_pk_f16_f32 v15, v24, v25
	ds_write_b128 v173, v[12:15] offset:64
	ds_read_b128 v[12:15], v174
	ds_read_b128 v[20:23], v174 offset:1152
	v_add_u32_e32 v24, s64, v40
	v_lshlrev_b32_e32 v25, 1, v24
	v_add_u32_e32 v26, v25, v168
	s_waitcnt lgkmcnt(1)
	buffer_store_dwordx4 v[12:15], v26, s[20:23], 0 offen
	v_pk_fma_f32 v[6:7], v[6:7], v[232:233], v[244:245] op_sel:[0,1,0]
	v_pk_fma_f32 v[4:5], v[4:5], v[232:233], v[242:243] op_sel:[0,1,0]
	v_pk_fma_f32 v[12:13], v[18:19], v[232:233], v[236:237] op_sel:[0,1,0]
	v_pk_fma_f32 v[14:15], v[16:17], v[232:233], v[234:235] op_sel:[0,1,0]
	v_pk_fma_f32 v[16:17], v[10:11], v[232:233], v[240:241] op_sel:[0,1,0]
	v_pk_fma_f32 v[10:11], v[8:9], v[232:233], v[238:239] op_sel:[0,1,0]
	v_cvt_pk_f16_f32 v8, v14, v15
	v_cvt_pk_f16_f32 v9, v12, v13
	v_cvt_pk_f16_f32 v10, v10, v11
	v_cvt_pk_f16_f32 v11, v16, v17
	ds_write_b128 v173, v[8:11]
	v_pk_fma_f32 v[8:9], v[2:3], v[232:233], v[248:249] op_sel:[0,1,0]
	v_pk_fma_f32 v[2:3], v[0:1], v[232:233], v[246:247] op_sel:[0,1,0]
	v_cvt_pk_f16_f32 v0, v4, v5
	v_cvt_pk_f16_f32 v1, v6, v7
	v_cvt_pk_f16_f32 v2, v2, v3
	v_cvt_pk_f16_f32 v3, v8, v9
	ds_write_b128 v173, v[0:3] offset:64
	ds_read_b128 v[0:3], v174
	ds_read_b128 v[4:7], v174 offset:1152
	v_add_lshl_u32 v8, v24, s64, 1
	v_add_u32_e32 v25, v25, v169
	v_add_u32_e32 v9, v8, v168
	s_waitcnt lgkmcnt(4)
	buffer_store_dwordx4 v[20:23], v25, s[20:23], 0 offen
	s_waitcnt lgkmcnt(1)
	buffer_store_dwordx4 v[0:3], v9, s[20:23], 0 offen
	s_mov_b32 s67, s68
	s_mov_b32 s70, s69
	v_add_u32_e32 v0, v8, v169
	s_mov_b64 s[30:31], s[0:1]
	s_mov_b64 s[28:29], s[8:9]
	s_mov_b64 vcc, s[6:7]
	s_waitcnt lgkmcnt(0)
	buffer_store_dwordx4 v[4:7], v0, s[20:23], 0 offen
	s_cbranch_vccz .LBB7_12
	s_waitcnt vmcnt(0)
	s_cmpk_gt_u32 s36, 0xff
	s_cbranch_scc1 .LBB7_31
	s_barrier

.LBB9_27:
	ds_read_b128 v[128:131], v172
	ds_read_b128 v[132:135], v172 offset:1024
	ds_read_b128 v[136:139], v172 offset:2048
	ds_read_b128 v[140:143], v172 offset:3072
	s_add_u32 s30, s28, 0xfffd0080
	s_addc_u32 s31, s29, -1
	s_cmp_eq_u32 s73, 8
	s_cselect_b32 s35, s9, s31
	s_cselect_b32 s34, s8, s30
	s_cselect_b32 s31, s1, s72
	s_cselect_b32 s30, s0, s71
	v_lshl_add_u64 v[202:203], s[28:29], 0, v[152:153]
	s_add_i32 m0, s43, 0xc000
	ds_read_b128 v[158:161], v173
	ds_read_b128 v[162:165], v173 offset:1024
	ds_read_b128 v[178:181], v173 offset:2048
	ds_read_b128 v[182:185], v173 offset:3072
	ds_read_b128 v[186:189], v173 offset:4096
	ds_read_b128 v[190:193], v173 offset:5120
	ds_read_b128 v[194:197], v173 offset:6144
	ds_read_b128 v[198:201], v173 offset:7168
	global_load_lds_dwordx4 v[202:203], off
	v_lshl_add_u64 v[202:203], s[28:29], 0, v[154:155]
	s_add_i32 m0, s43, 0xe000
	s_nop 0
	global_load_lds_dwordx4 v[202:203], off
	s_waitcnt lgkmcnt(8)
	s_barrier
	s_waitcnt lgkmcnt(0)
	s_setprio 1
	s_waitcnt lgkmcnt(0)
	v_mfma_f32_16x16x32_f16 v[124:127], v[128:131], v[158:161], v[124:127]
	v_mfma_f32_16x16x32_f16 v[120:123], v[136:139], v[158:161], v[120:123]
	v_mfma_f32_16x16x32_f16 v[108:111], v[128:131], v[178:181], v[108:111]
	v_mfma_f32_16x16x32_f16 v[104:107], v[136:139], v[178:181], v[104:107]
	v_mfma_f32_16x16x32_f16 v[96:99], v[128:131], v[186:189], v[96:99]
	v_mfma_f32_16x16x32_f16 v[88:91], v[136:139], v[186:189], v[88:91]
	v_mfma_f32_16x16x32_f16 v[80:83], v[128:131], v[194:197], v[80:83]
	v_mfma_f32_16x16x32_f16 v[72:75], v[136:139], v[194:197], v[72:75]
	v_mfma_f32_16x16x32_f16 v[124:127], v[132:135], v[162:165], v[124:127]
	v_mfma_f32_16x16x32_f16 v[120:123], v[140:143], v[162:165], v[120:123]
	v_mfma_f32_16x16x32_f16 v[108:111], v[132:135], v[182:185], v[108:111]
	v_mfma_f32_16x16x32_f16 v[104:107], v[140:143], v[182:185], v[104:107]
	v_mfma_f32_16x16x32_f16 v[96:99], v[132:135], v[190:193], v[96:99]
	v_mfma_f32_16x16x32_f16 v[88:91], v[140:143], v[190:193], v[88:91]
	v_mfma_f32_16x16x32_f16 v[80:83], v[132:135], v[198:201], v[80:83]
	v_mfma_f32_16x16x32_f16 v[72:75], v[140:143], v[198:201], v[72:75]
	s_setprio 0
	s_barrier
	s_add_i32 s74, s65, s42
	v_lshl_add_u64 v[218:219], s[30:31], 0, v[146:147]
	s_mov_b32 m0, s74
	ds_read_b128 v[202:205], v174
	ds_read_b128 v[206:209], v174 offset:1024
	ds_read_b128 v[210:213], v174 offset:2048
	ds_read_b128 v[214:217], v174 offset:3072
	global_load_lds_dwordx4 v[218:219], off
	v_lshl_add_u64 v[220:221], s[30:31], 0, v[150:151]
	s_add_i32 m0, s74, 0x2000
	s_nop 0
	global_load_lds_dwordx4 v[220:221], off
	s_barrier
	s_waitcnt lgkmcnt(0)
	s_setprio 1
	s_waitcnt lgkmcnt(0)
	v_mfma_f32_16x16x32_f16 v[116:119], v[202:205], v[158:161], v[116:119]
	v_mfma_f32_16x16x32_f16 v[112:115], v[210:213], v[158:161], v[112:115]
	v_mfma_f32_16x16x32_f16 v[100:103], v[202:205], v[178:181], v[100:103]
	v_mfma_f32_16x16x32_f16 v[92:95], v[210:213], v[178:181], v[92:95]
	v_mfma_f32_16x16x32_f16 v[84:87], v[202:205], v[186:189], v[84:87]
	v_mfma_f32_16x16x32_f16 v[76:79], v[210:213], v[186:189], v[76:79]
	v_mfma_f32_16x16x32_f16 v[68:71], v[202:205], v[194:197], v[68:71]
	v_mfma_f32_16x16x32_f16 v[64:67], v[210:213], v[194:197], v[64:67]
	v_mfma_f32_16x16x32_f16 v[116:119], v[206:209], v[162:165], v[116:119]
	v_mfma_f32_16x16x32_f16 v[112:115], v[214:217], v[162:165], v[112:115]
	v_mfma_f32_16x16x32_f16 v[100:103], v[206:209], v[182:185], v[100:103]
	v_mfma_f32_16x16x32_f16 v[92:95], v[214:217], v[182:185], v[92:95]
	v_mfma_f32_16x16x32_f16 v[84:87], v[206:209], v[190:193], v[84:87]
	v_mfma_f32_16x16x32_f16 v[76:79], v[214:217], v[190:193], v[76:79]
	v_mfma_f32_16x16x32_f16 v[68:71], v[206:209], v[198:201], v[68:71]
	v_mfma_f32_16x16x32_f16 v[64:67], v[214:217], v[198:201], v[64:67]
	s_setprio 0
	s_mov_b32 m0, s43
	v_lshl_add_u64 v[222:223], s[34:35], 0, v[144:145]
	s_barrier
	ds_read_b128 v[158:161], v173 offset:16384
	ds_read_b128 v[162:165], v173 offset:17408
	ds_read_b128 v[178:181], v173 offset:18432
	ds_read_b128 v[182:185], v173 offset:19456
	ds_read_b128 v[186:189], v173 offset:20480
	ds_read_b128 v[190:193], v173 offset:21504
	ds_read_b128 v[194:197], v173 offset:22528
	ds_read_b128 v[198:201], v173 offset:23552
	global_load_lds_dwordx4 v[222:223], off
	v_lshl_add_u64 v[224:225], s[34:35], 0, v[148:149]
	s_mov_b32 m0, s44
	s_nop 0
	global_load_lds_dwordx4 v[224:225], off
	s_barrier
	s_waitcnt lgkmcnt(0)
	s_setprio 1
	s_waitcnt lgkmcnt(0)
	v_mfma_f32_16x16x32_f16 v[60:63], v[128:131], v[158:161], v[60:63]
	v_mfma_f32_16x16x32_f16 v[56:59], v[136:139], v[158:161], v[56:59]
	v_mfma_f32_16x16x32_f16 v[48:51], v[128:131], v[178:181], v[48:51]
	v_mfma_f32_16x16x32_f16 v[40:43], v[136:139], v[178:181], v[40:43]
	v_mfma_f32_16x16x32_f16 v[32:35], v[128:131], v[186:189], v[32:35]
	v_mfma_f32_16x16x32_f16 v[24:27], v[136:139], v[186:189], v[24:27]
	v_mfma_f32_16x16x32_f16 v[16:19], v[128:131], v[194:197], v[16:19]
	v_mfma_f32_16x16x32_f16 v[8:11], v[136:139], v[194:197], v[8:11]
	v_mfma_f32_16x16x32_f16 v[60:63], v[132:135], v[162:165], v[60:63]
	v_mfma_f32_16x16x32_f16 v[56:59], v[140:143], v[162:165], v[56:59]
	v_mfma_f32_16x16x32_f16 v[48:51], v[132:135], v[182:185], v[48:51]
	v_mfma_f32_16x16x32_f16 v[40:43], v[140:143], v[182:185], v[40:43]
	v_mfma_f32_16x16x32_f16 v[32:35], v[132:135], v[190:193], v[32:35]
	v_mfma_f32_16x16x32_f16 v[24:27], v[140:143], v[190:193], v[24:27]
	v_mfma_f32_16x16x32_f16 v[16:19], v[132:135], v[198:201], v[16:19]
	v_mfma_f32_16x16x32_f16 v[8:11], v[140:143], v[198:201], v[8:11]
	s_setprio 0
	s_barrier
	s_add_u32 s74, s30, 0xc000
	s_addc_u32 s75, s31, 0
	s_add_i32 s76, s66, s42
	v_lshl_add_u64 v[128:129], s[74:75], 0, v[146:147]
	s_mov_b32 m0, s76
	s_nop 0
	global_load_lds_dwordx4 v[128:129], off
	v_lshl_add_u64 v[128:129], s[74:75], 0, v[150:151]
	s_add_i32 m0, s76, 0x2000
	s_nop 0
	global_load_lds_dwordx4 v[128:129], off
	s_waitcnt vmcnt(6)
	s_barrier
	s_setprio 1
	v_mfma_f32_16x16x32_f16 v[52:55], v[202:205], v[158:161], v[52:55]
	v_mfma_f32_16x16x32_f16 v[44:47], v[210:213], v[158:161], v[44:47]
	v_mfma_f32_16x16x32_f16 v[36:39], v[202:205], v[178:181], v[36:39]
	v_mfma_f32_16x16x32_f16 v[28:31], v[210:213], v[178:181], v[28:31]
	v_mfma_f32_16x16x32_f16 v[20:23], v[202:205], v[186:189], v[20:23]
	v_mfma_f32_16x16x32_f16 v[12:15], v[210:213], v[186:189], v[12:15]
	v_mfma_f32_16x16x32_f16 v[4:7], v[202:205], v[194:197], v[4:7]
	v_mfma_f32_16x16x32_f16 v[0:3], v[210:213], v[194:197], v[0:3]
	v_mfma_f32_16x16x32_f16 v[52:55], v[206:209], v[162:165], v[52:55]
	v_mfma_f32_16x16x32_f16 v[44:47], v[214:217], v[162:165], v[44:47]
	v_mfma_f32_16x16x32_f16 v[36:39], v[206:209], v[182:185], v[36:39]
	v_mfma_f32_16x16x32_f16 v[28:31], v[214:217], v[182:185], v[28:31]
	v_mfma_f32_16x16x32_f16 v[20:23], v[206:209], v[190:193], v[20:23]
	v_mfma_f32_16x16x32_f16 v[12:15], v[214:217], v[190:193], v[12:15]
	v_mfma_f32_16x16x32_f16 v[4:7], v[206:209], v[198:201], v[4:7]
	v_mfma_f32_16x16x32_f16 v[0:3], v[214:217], v[198:201], v[0:3]
	s_setprio 0
	s_add_i32 s74, 0, 0x18000
	v_add_u32_e32 v140, s74, v168
	s_barrier
	ds_read_b128 v[128:131], v140
	ds_read_b128 v[132:135], v140 offset:1024
	ds_read_b128 v[136:139], v140 offset:2048
	ds_read_b128 v[140:143], v140 offset:3072
	s_add_u32 s34, s34, 0x30000
	s_addc_u32 s35, s35, 0
	s_mov_b32 m0, s45
	v_lshl_add_u64 v[202:203], s[34:35], 0, v[144:145]
	ds_read_b128 v[158:161], v173 offset:32768
	ds_read_b128 v[162:165], v173 offset:33792
	ds_read_b128 v[178:181], v173 offset:34816
	ds_read_b128 v[182:185], v173 offset:35840
	ds_read_b128 v[186:189], v173 offset:36864
	ds_read_b128 v[190:193], v173 offset:37888
	ds_read_b128 v[194:197], v173 offset:38912
	ds_read_b128 v[198:201], v173 offset:39936
	global_load_lds_dwordx4 v[202:203], off
	v_lshl_add_u64 v[202:203], s[34:35], 0, v[148:149]
	s_mov_b32 m0, s46
	s_nop 0
	global_load_lds_dwordx4 v[202:203], off
	s_waitcnt lgkmcnt(8)
	s_barrier
	s_waitcnt lgkmcnt(0)
	s_setprio 1
	s_waitcnt lgkmcnt(0)
	v_mfma_f32_16x16x32_f16 v[124:127], v[128:131], v[158:161], v[124:127]
	v_mfma_f32_16x16x32_f16 v[120:123], v[136:139], v[158:161], v[120:123]
	v_mfma_f32_16x16x32_f16 v[108:111], v[128:131], v[178:181], v[108:111]
	v_mfma_f32_16x16x32_f16 v[104:107], v[136:139], v[178:181], v[104:107]
	v_mfma_f32_16x16x32_f16 v[96:99], v[128:131], v[186:189], v[96:99]
	v_mfma_f32_16x16x32_f16 v[88:91], v[136:139], v[186:189], v[88:91]
	v_mfma_f32_16x16x32_f16 v[80:83], v[128:131], v[194:197], v[80:83]
	v_mfma_f32_16x16x32_f16 v[72:75], v[136:139], v[194:197], v[72:75]
	v_mfma_f32_16x16x32_f16 v[124:127], v[132:135], v[162:165], v[124:127]
	v_mfma_f32_16x16x32_f16 v[120:123], v[140:143], v[162:165], v[120:123]
	v_mfma_f32_16x16x32_f16 v[108:111], v[132:135], v[182:185], v[108:111]
	v_mfma_f32_16x16x32_f16 v[104:107], v[140:143], v[182:185], v[104:107]
	v_mfma_f32_16x16x32_f16 v[96:99], v[132:135], v[190:193], v[96:99]
	v_mfma_f32_16x16x32_f16 v[88:91], v[140:143], v[190:193], v[88:91]
	v_mfma_f32_16x16x32_f16 v[80:83], v[132:135], v[198:201], v[80:83]
	v_mfma_f32_16x16x32_f16 v[72:75], v[140:143], v[198:201], v[72:75]
	s_setprio 0
	s_barrier
	s_add_i32 s34, 0, 0x1c000
	s_add_i32 s35, s74, s42
	v_add_u32_e32 v177, s34, v168
	v_lshl_add_u64 v[218:219], v[218:219], 0, s[26:27]
	s_mov_b32 m0, s35
	ds_read_b128 v[202:205], v177
	ds_read_b128 v[206:209], v177 offset:1024
	ds_read_b128 v[210:213], v177 offset:2048
	ds_read_b128 v[214:217], v177 offset:3072
	global_load_lds_dwordx4 v[218:219], off
	v_lshl_add_u64 v[218:219], v[220:221], 0, s[26:27]
	s_add_i32 m0, s35, 0x2000
	s_nop 0
	global_load_lds_dwordx4 v[218:219], off
	s_barrier
	s_waitcnt lgkmcnt(0)
	s_setprio 1
	s_waitcnt lgkmcnt(0)
	v_mfma_f32_16x16x32_f16 v[116:119], v[202:205], v[158:161], v[116:119]
	v_mfma_f32_16x16x32_f16 v[112:115], v[210:213], v[158:161], v[112:115]
	v_mfma_f32_16x16x32_f16 v[100:103], v[202:205], v[178:181], v[100:103]
	v_mfma_f32_16x16x32_f16 v[92:95], v[210:213], v[178:181], v[92:95]
	v_mfma_f32_16x16x32_f16 v[84:87], v[202:205], v[186:189], v[84:87]
	v_mfma_f32_16x16x32_f16 v[76:79], v[210:213], v[186:189], v[76:79]
	v_mfma_f32_16x16x32_f16 v[68:71], v[202:205], v[194:197], v[68:71]
	v_mfma_f32_16x16x32_f16 v[64:67], v[210:213], v[194:197], v[64:67]
	v_mfma_f32_16x16x32_f16 v[116:119], v[206:209], v[162:165], v[116:119]
	v_mfma_f32_16x16x32_f16 v[112:115], v[214:217], v[162:165], v[112:115]
	v_mfma_f32_16x16x32_f16 v[100:103], v[206:209], v[182:185], v[100:103]
	v_mfma_f32_16x16x32_f16 v[92:95], v[214:217], v[182:185], v[92:95]
	v_mfma_f32_16x16x32_f16 v[84:87], v[206:209], v[190:193], v[84:87]
	v_mfma_f32_16x16x32_f16 v[76:79], v[214:217], v[190:193], v[76:79]
	v_mfma_f32_16x16x32_f16 v[68:71], v[206:209], v[198:201], v[68:71]
	v_mfma_f32_16x16x32_f16 v[64:67], v[214:217], v[198:201], v[64:67]
	s_setprio 0
	s_mov_b32 m0, s49
	v_lshl_add_u64 v[218:219], v[222:223], 0, s[26:27]
	s_barrier
	ds_read_b128 v[158:161], v173 offset:49152
	ds_read_b128 v[162:165], v173 offset:50176
	ds_read_b128 v[178:181], v173 offset:51200
	ds_read_b128 v[182:185], v173 offset:52224
	ds_read_b128 v[186:189], v173 offset:53248
	ds_read_b128 v[190:193], v173 offset:54272
	ds_read_b128 v[194:197], v173 offset:55296
	ds_read_b128 v[198:201], v173 offset:56320
	global_load_lds_dwordx4 v[218:219], off
	v_lshl_add_u64 v[218:219], v[224:225], 0, s[26:27]
	s_mov_b32 m0, s50
	s_nop 0
	global_load_lds_dwordx4 v[218:219], off
	s_barrier
	s_waitcnt lgkmcnt(0)
	s_setprio 1
	s_waitcnt lgkmcnt(0)
	v_mfma_f32_16x16x32_f16 v[60:63], v[128:131], v[158:161], v[60:63]
	v_mfma_f32_16x16x32_f16 v[56:59], v[136:139], v[158:161], v[56:59]
	v_mfma_f32_16x16x32_f16 v[48:51], v[128:131], v[178:181], v[48:51]
	v_mfma_f32_16x16x32_f16 v[40:43], v[136:139], v[178:181], v[40:43]
	v_mfma_f32_16x16x32_f16 v[32:35], v[128:131], v[186:189], v[32:35]
	v_mfma_f32_16x16x32_f16 v[24:27], v[136:139], v[186:189], v[24:27]
	v_mfma_f32_16x16x32_f16 v[16:19], v[128:131], v[194:197], v[16:19]
	v_mfma_f32_16x16x32_f16 v[8:11], v[136:139], v[194:197], v[8:11]
	v_mfma_f32_16x16x32_f16 v[60:63], v[132:135], v[162:165], v[60:63]
	v_mfma_f32_16x16x32_f16 v[56:59], v[140:143], v[162:165], v[56:59]
	v_mfma_f32_16x16x32_f16 v[48:51], v[132:135], v[182:185], v[48:51]
	v_mfma_f32_16x16x32_f16 v[40:43], v[140:143], v[182:185], v[40:43]
	v_mfma_f32_16x16x32_f16 v[32:35], v[132:135], v[190:193], v[32:35]
	v_mfma_f32_16x16x32_f16 v[24:27], v[140:143], v[190:193], v[24:27]
	v_mfma_f32_16x16x32_f16 v[16:19], v[132:135], v[198:201], v[16:19]
	v_mfma_f32_16x16x32_f16 v[8:11], v[140:143], v[198:201], v[8:11]
	s_setprio 0
	s_barrier
	s_add_u32 s30, s30, 0xc080
	s_addc_u32 s31, s31, 0
	s_add_i32 s34, s34, s42
	v_lshl_add_u64 v[128:129], s[30:31], 0, v[146:147]
	s_mov_b32 m0, s34
	s_nop 0
	global_load_lds_dwordx4 v[128:129], off
	v_lshl_add_u64 v[128:129], s[30:31], 0, v[150:151]
	s_add_i32 m0, s34, 0x2000
	s_nop 0
	global_load_lds_dwordx4 v[128:129], off
	s_waitcnt vmcnt(6)
	s_barrier
	s_setprio 1
	v_mfma_f32_16x16x32_f16 v[52:55], v[202:205], v[158:161], v[52:55]
	v_mfma_f32_16x16x32_f16 v[44:47], v[210:213], v[158:161], v[44:47]
	v_mfma_f32_16x16x32_f16 v[36:39], v[202:205], v[178:181], v[36:39]
	v_mfma_f32_16x16x32_f16 v[28:31], v[210:213], v[178:181], v[28:31]
	v_mfma_f32_16x16x32_f16 v[20:23], v[202:205], v[186:189], v[20:23]
	v_mfma_f32_16x16x32_f16 v[12:15], v[210:213], v[186:189], v[12:15]
	v_mfma_f32_16x16x32_f16 v[4:7], v[202:205], v[194:197], v[4:7]
	v_mfma_f32_16x16x32_f16 v[0:3], v[210:213], v[194:197], v[0:3]
	v_mfma_f32_16x16x32_f16 v[52:55], v[206:209], v[162:165], v[52:55]
	v_mfma_f32_16x16x32_f16 v[44:47], v[214:217], v[162:165], v[44:47]
	v_mfma_f32_16x16x32_f16 v[36:39], v[206:209], v[182:185], v[36:39]
	v_mfma_f32_16x16x32_f16 v[28:31], v[214:217], v[182:185], v[28:31]
	v_mfma_f32_16x16x32_f16 v[20:23], v[206:209], v[190:193], v[20:23]
	v_mfma_f32_16x16x32_f16 v[12:15], v[214:217], v[190:193], v[12:15]
	v_mfma_f32_16x16x32_f16 v[4:7], v[206:209], v[198:201], v[4:7]
	v_mfma_f32_16x16x32_f16 v[0:3], v[214:217], v[198:201], v[0:3]
	s_setprio 0
	s_add_i32 s73, s73, 2
	s_add_u32 s28, s28, 0x100
	s_addc_u32 s29, s29, 0
	s_add_u32 s71, s71, 0x100
	s_addc_u32 s72, s72, 0
	s_cmp_gt_u32 s73, 9
	s_barrier
	s_cbranch_scc0 .LBB9_27
	s_lshl_b32 s28, s70, 8
	s_add_i32 s28, s28, s48
	s_lshl_b32 s29, s68, 8
	s_or_b32 s29, s29, s51
	s_waitcnt vmcnt(6)
	v_pk_fma_f32 v[126:127], v[126:127], v[226:227], v[236:237] op_sel_hi:[1,0,1]
	v_pk_fma_f32 v[124:125], v[124:125], v[226:227], v[234:235] op_sel_hi:[1,0,1]
	v_pk_fma_f32 v[122:123], v[122:123], v[226:227], v[240:241] op_sel_hi:[1,0,1]
	v_pk_fma_f32 v[120:121], v[120:121], v[226:227], v[238:239] op_sel_hi:[1,0,1]
	v_cvt_pk_f16_f32 v124, v124, v125
	v_cvt_pk_f16_f32 v125, v126, v127
	v_cvt_pk_f16_f32 v126, v120, v121
	v_cvt_pk_f16_f32 v123, v122, v123
	v_pk_fma_f32 v[118:119], v[118:119], v[226:227], v[244:245] op_sel_hi:[1,0,1]
	v_pk_fma_f32 v[116:117], v[116:117], v[226:227], v[242:243] op_sel_hi:[1,0,1]
	v_pk_fma_f32 v[114:115], v[114:115], v[226:227], v[248:249] op_sel_hi:[1,0,1]
	v_pk_fma_f32 v[112:113], v[112:113], v[226:227], v[246:247] op_sel_hi:[1,0,1]
	v_pk_max_f16 v120, v124, 0
	v_pk_max_f16 v121, v125, 0
	v_pk_max_f16 v122, v126, 0
	v_pk_max_f16 v123, v123, 0
	v_cvt_pk_f16_f32 v116, v116, v117
	v_cvt_pk_f16_f32 v117, v118, v119
	v_cvt_pk_f16_f32 v118, v112, v113
	v_cvt_pk_f16_f32 v115, v114, v115
	v_pk_fma_f32 v[110:111], v[110:111], v[226:227], v[236:237] op_sel:[0,1,0]
	v_pk_fma_f32 v[108:109], v[108:109], v[226:227], v[234:235] op_sel:[0,1,0]
	v_pk_fma_f32 v[106:107], v[106:107], v[226:227], v[240:241] op_sel:[0,1,0]
	v_pk_fma_f32 v[104:105], v[104:105], v[226:227], v[238:239] op_sel:[0,1,0]
	v_pk_fma_f32 v[102:103], v[102:103], v[226:227], v[244:245] op_sel:[0,1,0]
	v_pk_fma_f32 v[100:101], v[100:101], v[226:227], v[242:243] op_sel:[0,1,0]
	v_pk_fma_f32 v[94:95], v[94:95], v[226:227], v[248:249] op_sel:[0,1,0]
	v_pk_fma_f32 v[92:93], v[92:93], v[226:227], v[246:247] op_sel:[0,1,0]
	ds_write_b128 v175, v[120:123]
	v_or_b32_e32 v120, s28, v169
	v_pk_max_f16 v112, v116, 0
	v_pk_max_f16 v113, v117, 0
	v_pk_max_f16 v114, v118, 0
	v_pk_max_f16 v115, v115, 0
	v_cvt_pk_f16_f32 v108, v108, v109
	v_cvt_pk_f16_f32 v109, v110, v111
	v_cvt_pk_f16_f32 v110, v104, v105
	v_cvt_pk_f16_f32 v107, v106, v107
	v_cvt_pk_f16_f32 v100, v100, v101
	v_cvt_pk_f16_f32 v101, v102, v103
	v_cvt_pk_f16_f32 v102, v92, v93
	v_cvt_pk_f16_f32 v95, v94, v95
	ds_write_b128 v175, v[112:115] offset:64
	v_mul_lo_u32 v116, v120, s10
	v_pk_max_f16 v104, v108, 0
	v_pk_max_f16 v105, v109, 0
	v_pk_max_f16 v106, v110, 0
	v_pk_max_f16 v107, v107, 0
	v_pk_max_f16 v92, v100, 0
	v_pk_max_f16 v93, v101, 0
	v_pk_max_f16 v94, v102, 0
	v_pk_max_f16 v95, v95, 0
	ds_read_b128 v[112:115], v176
	v_add_u32_e32 v120, s29, v116
	ds_read_b128 v[116:119], v176 offset:1152
	ds_write_b128 v175, v[104:107]
	ds_write_b128 v175, v[92:95] offset:64
	ds_read_b128 v[92:95], v176
	ds_read_b128 v[100:103], v176 offset:1152
	v_lshlrev_b32_e32 v121, 1, v120
	v_add_u32_e32 v122, v121, v170
	v_add_u32_e32 v104, s55, v121
	s_waitcnt lgkmcnt(0)
	buffer_store_dwordx4 v[112:115], v122, s[20:23], 0 offen
	v_add_u32_e32 v105, v104, v170
	v_pk_fma_f32 v[90:91], v[90:91], v[228:229], v[240:241] op_sel_hi:[1,0,1]
	v_add_u32_e32 v112, v121, v171
	buffer_store_dwordx4 v[116:119], v112, s[20:23], 0 offen
	buffer_store_dwordx4 v[92:95], v105, s[20:23], 0 offen
	v_pk_fma_f32 v[88:89], v[88:89], v[228:229], v[238:239] op_sel_hi:[1,0,1]
	v_pk_fma_f32 v[86:87], v[86:87], v[228:229], v[244:245] op_sel_hi:[1,0,1]
	v_pk_fma_f32 v[92:93], v[98:99], v[228:229], v[236:237] op_sel_hi:[1,0,1]
	v_pk_fma_f32 v[94:95], v[96:97], v[228:229], v[234:235] op_sel_hi:[1,0,1]
	v_pk_fma_f32 v[84:85], v[84:85], v[228:229], v[242:243] op_sel_hi:[1,0,1]
	v_pk_fma_f32 v[78:79], v[78:79], v[228:229], v[248:249] op_sel_hi:[1,0,1]
	v_pk_fma_f32 v[76:77], v[76:77], v[228:229], v[246:247] op_sel_hi:[1,0,1]
	v_cvt_pk_f16_f32 v94, v94, v95
	v_cvt_pk_f16_f32 v92, v92, v93
	v_cvt_pk_f16_f32 v93, v88, v89
	v_cvt_pk_f16_f32 v91, v90, v91
	v_cvt_pk_f16_f32 v84, v84, v85
	v_cvt_pk_f16_f32 v85, v86, v87
	v_cvt_pk_f16_f32 v86, v76, v77
	v_cvt_pk_f16_f32 v79, v78, v79
	v_pk_max_f16 v88, v94, 0
	v_pk_max_f16 v89, v92, 0
	v_pk_max_f16 v90, v93, 0
	v_pk_max_f16 v91, v91, 0
	v_pk_max_f16 v76, v84, 0
	v_pk_max_f16 v77, v85, 0
	v_pk_max_f16 v78, v86, 0
	v_pk_max_f16 v79, v79, 0
	ds_write_b128 v175, v[88:91]
	ds_write_b128 v175, v[76:79] offset:64
	ds_read_b128 v[76:79], v176
	ds_read_b128 v[84:87], v176 offset:1152
	v_add_u32_e32 v88, s55, v104
	v_add_u32_e32 v105, v104, v171
	v_add_u32_e32 v89, v88, v170
	buffer_store_dwordx4 v[100:103], v105, s[20:23], 0 offen
	s_waitcnt lgkmcnt(1)
	buffer_store_dwordx4 v[76:79], v89, s[20:23], 0 offen
	v_pk_fma_f32 v[74:75], v[74:75], v[228:229], v[240:241] op_sel:[0,1,0]
	v_pk_fma_f32 v[72:73], v[72:73], v[228:229], v[238:239] op_sel:[0,1,0]
	v_add_u32_e32 v76, v88, v171
	s_waitcnt lgkmcnt(0)
	buffer_store_dwordx4 v[84:87], v76, s[20:23], 0 offen
	v_pk_fma_f32 v[76:77], v[82:83], v[228:229], v[236:237] op_sel:[0,1,0]
	v_pk_fma_f32 v[78:79], v[80:81], v[228:229], v[234:235] op_sel:[0,1,0]
	v_pk_fma_f32 v[70:71], v[70:71], v[228:229], v[244:245] op_sel:[0,1,0]
	v_pk_fma_f32 v[68:69], v[68:69], v[228:229], v[242:243] op_sel:[0,1,0]
	v_pk_fma_f32 v[66:67], v[66:67], v[228:229], v[248:249] op_sel:[0,1,0]
	v_pk_fma_f32 v[64:65], v[64:65], v[228:229], v[246:247] op_sel:[0,1,0]
	v_cvt_pk_f16_f32 v78, v78, v79
	v_cvt_pk_f16_f32 v76, v76, v77
	v_cvt_pk_f16_f32 v77, v72, v73
	v_cvt_pk_f16_f32 v75, v74, v75
	v_cvt_pk_f16_f32 v68, v68, v69
	v_cvt_pk_f16_f32 v69, v70, v71
	v_cvt_pk_f16_f32 v70, v64, v65
	v_cvt_pk_f16_f32 v67, v66, v67
	v_pk_fma_f32 v[62:63], v[62:63], v[230:231], v[236:237] op_sel_hi:[1,0,1]
	v_pk_fma_f32 v[60:61], v[60:61], v[230:231], v[234:235] op_sel_hi:[1,0,1]
	v_pk_fma_f32 v[58:59], v[58:59], v[230:231], v[240:241] op_sel_hi:[1,0,1]
	v_pk_fma_f32 v[56:57], v[56:57], v[230:231], v[238:239] op_sel_hi:[1,0,1]
	v_pk_fma_f32 v[54:55], v[54:55], v[230:231], v[244:245] op_sel_hi:[1,0,1]
	v_pk_fma_f32 v[52:53], v[52:53], v[230:231], v[242:243] op_sel_hi:[1,0,1]
	v_pk_fma_f32 v[46:47], v[46:47], v[230:231], v[248:249] op_sel_hi:[1,0,1]
	v_pk_fma_f32 v[44:45], v[44:45], v[230:231], v[246:247] op_sel_hi:[1,0,1]
	v_pk_max_f16 v72, v78, 0
	v_pk_max_f16 v73, v76, 0
	v_pk_max_f16 v74, v77, 0
	v_pk_max_f16 v75, v75, 0
	v_pk_max_f16 v64, v68, 0
	v_pk_max_f16 v65, v69, 0
	v_pk_max_f16 v66, v70, 0
	v_pk_max_f16 v67, v67, 0
	v_cvt_pk_f16_f32 v60, v60, v61
	v_cvt_pk_f16_f32 v61, v62, v63
	v_cvt_pk_f16_f32 v62, v56, v57
	v_cvt_pk_f16_f32 v59, v58, v59
	v_cvt_pk_f16_f32 v52, v52, v53
	v_cvt_pk_f16_f32 v53, v54, v55
	v_cvt_pk_f16_f32 v54, v44, v45
	v_cvt_pk_f16_f32 v47, v46, v47
	ds_write_b128 v175, v[72:75]
	ds_write_b128 v175, v[64:67] offset:64
	v_pk_max_f16 v56, v60, 0
	v_pk_max_f16 v57, v61, 0
	v_pk_max_f16 v58, v62, 0
	v_pk_max_f16 v59, v59, 0
	v_pk_max_f16 v44, v52, 0
	v_pk_max_f16 v45, v53, 0
	v_pk_max_f16 v46, v54, 0
	v_pk_max_f16 v47, v47, 0
	ds_read_b128 v[64:67], v176
	ds_read_b128 v[68:71], v176 offset:1152
	ds_write_b128 v175, v[56:59]
	ds_write_b128 v175, v[44:47] offset:64
	ds_read_b128 v[44:47], v176
	ds_read_b128 v[52:55], v176 offset:1152
	v_add_u32_e32 v72, s56, v120
	v_lshlrev_b32_e32 v73, 1, v72
	v_add_u32_e32 v74, v73, v170
	v_add_u32_e32 v56, s62, v88
	s_waitcnt lgkmcnt(5)
	buffer_store_dwordx4 v[64:67], v74, s[20:23], 0 offen
	v_add_u32_e32 v57, v56, v170
	v_pk_fma_f32 v[42:43], v[42:43], v[230:231], v[240:241] op_sel:[0,1,0]
	v_add_u32_e32 v64, v73, v171
	s_waitcnt lgkmcnt(4)
	buffer_store_dwordx4 v[68:71], v64, s[20:23], 0 offen
	s_waitcnt lgkmcnt(1)
	buffer_store_dwordx4 v[44:47], v57, s[20:23], 0 offen
	v_pk_fma_f32 v[40:41], v[40:41], v[230:231], v[238:239] op_sel:[0,1,0]
	v_pk_fma_f32 v[38:39], v[38:39], v[230:231], v[244:245] op_sel:[0,1,0]
	v_add_u32_e32 v44, v56, v171
	s_waitcnt lgkmcnt(0)
	buffer_store_dwordx4 v[52:55], v44, s[20:23], 0 offen
	v_pk_fma_f32 v[44:45], v[50:51], v[230:231], v[236:237] op_sel:[0,1,0]
	v_pk_fma_f32 v[46:47], v[48:49], v[230:231], v[234:235] op_sel:[0,1,0]
	v_pk_fma_f32 v[36:37], v[36:37], v[230:231], v[242:243] op_sel:[0,1,0]
	v_pk_fma_f32 v[30:31], v[30:31], v[230:231], v[248:249] op_sel:[0,1,0]
	v_pk_fma_f32 v[28:29], v[28:29], v[230:231], v[246:247] op_sel:[0,1,0]
	v_cvt_pk_f16_f32 v46, v46, v47
	v_cvt_pk_f16_f32 v44, v44, v45
	v_cvt_pk_f16_f32 v45, v40, v41
	v_cvt_pk_f16_f32 v43, v42, v43
	v_cvt_pk_f16_f32 v36, v36, v37
	v_cvt_pk_f16_f32 v37, v38, v39
	v_cvt_pk_f16_f32 v38, v28, v29
	v_cvt_pk_f16_f32 v31, v30, v31
	v_pk_max_f16 v40, v46, 0
	v_pk_max_f16 v41, v44, 0
	v_pk_max_f16 v42, v45, 0
	v_pk_max_f16 v43, v43, 0
	v_pk_max_f16 v28, v36, 0
	v_pk_max_f16 v29, v37, 0
	v_pk_max_f16 v30, v38, 0
	v_pk_max_f16 v31, v31, 0
	ds_write_b128 v175, v[40:43]
	ds_write_b128 v175, v[28:31] offset:64
	ds_read_b128 v[28:31], v176
	ds_read_b128 v[36:39], v176 offset:1152
	v_add_u32_e32 v40, s63, v72
	v_lshlrev_b32_e32 v41, 1, v40
	v_add_u32_e32 v42, v41, v170
	s_waitcnt lgkmcnt(1)
	buffer_store_dwordx4 v[28:31], v42, s[20:23], 0 offen
	v_pk_fma_f32 v[26:27], v[26:27], v[232:233], v[240:241] op_sel_hi:[1,0,1]
	v_pk_fma_f32 v[24:25], v[24:25], v[232:233], v[238:239] op_sel_hi:[1,0,1]
	v_add_u32_e32 v28, v41, v171
	s_waitcnt lgkmcnt(0)
	buffer_store_dwordx4 v[36:39], v28, s[20:23], 0 offen
	v_pk_fma_f32 v[28:29], v[34:35], v[232:233], v[236:237] op_sel_hi:[1,0,1]
	v_pk_fma_f32 v[30:31], v[32:33], v[232:233], v[234:235] op_sel_hi:[1,0,1]
	v_pk_fma_f32 v[22:23], v[22:23], v[232:233], v[244:245] op_sel_hi:[1,0,1]
	v_pk_fma_f32 v[20:21], v[20:21], v[232:233], v[242:243] op_sel_hi:[1,0,1]
	v_pk_fma_f32 v[14:15], v[14:15], v[232:233], v[248:249] op_sel_hi:[1,0,1]
	v_pk_fma_f32 v[12:13], v[12:13], v[232:233], v[246:247] op_sel_hi:[1,0,1]
	v_cvt_pk_f16_f32 v30, v30, v31
	v_cvt_pk_f16_f32 v28, v28, v29
	v_cvt_pk_f16_f32 v29, v24, v25
	v_cvt_pk_f16_f32 v27, v26, v27
	v_cvt_pk_f16_f32 v20, v20, v21
	v_cvt_pk_f16_f32 v21, v22, v23
	v_cvt_pk_f16_f32 v22, v12, v13
	v_cvt_pk_f16_f32 v15, v14, v15
	v_pk_max_f16 v24, v30, 0
	v_pk_max_f16 v25, v28, 0
	v_pk_max_f16 v26, v29, 0
	v_pk_max_f16 v27, v27, 0
	v_pk_max_f16 v12, v20, 0
	v_pk_max_f16 v13, v21, 0
	v_pk_max_f16 v14, v22, 0
	v_pk_max_f16 v15, v15, 0
	ds_write_b128 v175, v[24:27]
	ds_write_b128 v175, v[12:15] offset:64
	ds_read_b128 v[12:15], v176
	ds_read_b128 v[20:23], v176 offset:1152
	v_add_u32_e32 v24, s64, v40
	v_lshlrev_b32_e32 v25, 1, v24
	v_add_u32_e32 v26, v25, v170
	s_waitcnt lgkmcnt(1)
	buffer_store_dwordx4 v[12:15], v26, s[20:23], 0 offen
	v_pk_fma_f32 v[10:11], v[10:11], v[232:233], v[240:241] op_sel:[0,1,0]
	v_pk_fma_f32 v[8:9], v[8:9], v[232:233], v[238:239] op_sel:[0,1,0]
	v_pk_fma_f32 v[12:13], v[18:19], v[232:233], v[236:237] op_sel:[0,1,0]
	v_pk_fma_f32 v[14:15], v[16:17], v[232:233], v[234:235] op_sel:[0,1,0]
	v_pk_fma_f32 v[6:7], v[6:7], v[232:233], v[244:245] op_sel:[0,1,0]
	v_pk_fma_f32 v[4:5], v[4:5], v[232:233], v[242:243] op_sel:[0,1,0]
	v_pk_fma_f32 v[2:3], v[2:3], v[232:233], v[248:249] op_sel:[0,1,0]
	v_pk_fma_f32 v[0:1], v[0:1], v[232:233], v[246:247] op_sel:[0,1,0]
	v_cvt_pk_f16_f32 v14, v14, v15
	v_cvt_pk_f16_f32 v12, v12, v13
	v_cvt_pk_f16_f32 v13, v8, v9
	v_cvt_pk_f16_f32 v11, v10, v11
	v_cvt_pk_f16_f32 v4, v4, v5
	v_cvt_pk_f16_f32 v5, v6, v7
	v_cvt_pk_f16_f32 v6, v0, v1
	v_cvt_pk_f16_f32 v3, v2, v3
	v_pk_max_f16 v8, v14, 0
	v_pk_max_f16 v9, v12, 0
	v_pk_max_f16 v10, v13, 0
	v_pk_max_f16 v11, v11, 0
	v_pk_max_f16 v0, v4, 0
	v_pk_max_f16 v1, v5, 0
	v_pk_max_f16 v2, v6, 0
	v_pk_max_f16 v3, v3, 0
	ds_write_b128 v175, v[8:11]
	ds_write_b128 v175, v[0:3] offset:64
	ds_read_b128 v[0:3], v176
	ds_read_b128 v[4:7], v176 offset:1152
	v_add_lshl_u32 v8, v24, s64, 1
	v_add_u32_e32 v25, v25, v171
	v_add_u32_e32 v9, v8, v170
	s_waitcnt lgkmcnt(4)
	buffer_store_dwordx4 v[20:23], v25, s[20:23], 0 offen
	s_waitcnt lgkmcnt(1)
	buffer_store_dwordx4 v[0:3], v9, s[20:23], 0 offen
	s_mov_b32 s68, s67
	s_mov_b32 s70, s69
	v_add_u32_e32 v0, v8, v171
	s_mov_b64 s[30:31], s[0:1]
	s_mov_b64 s[28:29], s[8:9]
	s_mov_b64 vcc, s[6:7]
	s_waitcnt lgkmcnt(0)
	buffer_store_dwordx4 v[4:7], v0, s[20:23], 0 offen
	s_cbranch_vccz .LBB9_12
	s_waitcnt vmcnt(0)
	s_cmpk_gt_u32 s36, 0xff
	s_cbranch_scc1 .LBB9_31
	s_barrier
